# 7 layer-0 tail items per wave in the attention stream (0x8800..0xbfff), block behind the 15th PV MFMA
# speedup vs baseline: 1.0129x; 1.0129x over previous
;     __device__ __forceinline__ const float* x() const { return (const float*)ld(0); }
; __device__ __forceinline__ void convert_moe_items(const Ctx& a, int layer, LAS unsigned char* lds, int it0, int it1, int widx, int nw, int wave, int lane) {
;     ...
;     int it = it0 + widx;
;     if (it >= it1) return;
;     f32x4 va[8], vb[8]; CvtItem da = decode(it), db = da; bool hb = (it + nw < it1);
;     cvt_load(da, va, lane);
;     if (hb) { db = decode(it + nw); cvt_load(db, vb, lane); }
; PHASE_FN ph_win() { PH_PRO;
;     ...
;     { const int nu = S.total(), maxu = (nu + G - 1) / G, nfull = nu - (maxu - 1) * G;
;       if ((int)blockIdx.x >= nfull && nfull < G) convert_moe_items(a, 0, lds, L0_B, MOE_ITEMS, ((int)blockIdx.x - nfull) * NWAVES + wave, (G - nfull) * NWAVES, wave, lane);
.LBB0_423:
	s_andn2_b64 vcc, exec, s[2:3]
	s_cbranch_vccnz .LBB0_471
	s_sub_i32 s0, s96, s29
	s_lshl_b32 s2, s0, 3
	s_add_i32 s0, 0, 0x23f10
	v_mov_b32_e32 v2, s0
	s_waitcnt vmcnt(0)
	ds_read_b64 v[6:7], v2
	s_add_i32 s0, 0, 0x23ee8
	v_mov_b32_e32 v2, s0
	s_add_i32 s0, 0, 0x23ef8
	ds_read2_b64 v[2:5], v2 offset1:1
	s_waitcnt lgkmcnt(1)
	v_readfirstlane_b32 s4, v6
	v_mov_b32_e32 v6, s0
	v_readfirstlane_b32 s3, v7
	ds_read_b64 v[6:7], v6
	s_add_i32 s2, s2, s58
	s_waitcnt lgkmcnt(1)
	v_readfirstlane_b32 s30, v3
	v_readfirstlane_b32 s31, v2
	v_readfirstlane_b32 s33, v5
	v_readfirstlane_b32 s34, v4
	s_waitcnt lgkmcnt(0)
	v_readfirstlane_b32 s35, v7
	s_cmpk_gt_u32 s2, 0x37ff
	v_readfirstlane_b32 s36, v6
	s_cbranch_scc1 .LBB0_471
	s_add_u32 s0, s4, 0x2530000
	s_addc_u32 s1, s3, 0
	s_add_u32 s4, s4, 0x12530000
	s_addc_u32 s5, s3, 0
	s_add_i32 s39, s2, 0x5000
	s_and_b32 s2, s39, 0xffff
	s_mul_i32 s2, s2, 0xaaab
	s_lshr_b32 s2, s2, 27
	s_mul_i32 s3, s2, 0xc00
	s_sub_i32 s3, s39, s3
	s_and_b32 s10, s3, 0xffff
	s_lshl_b32 s16, s2, 21
	s_lshl_b32 s11, s2, 11
	s_cmpk_gt_u32 s10, 0x3ff
	s_cbranch_scc0 .LBB0_430
	s_cmpk_gt_u32 s10, 0x7ff
	s_cbranch_scc0 .LBB0_436
	s_add_i32 s13, s10, 0xfffff800
	s_lshl_b32 s2, s16, 2
	s_add_u32 s2, s36, s2
	s_addc_u32 s3, s35, 0
	s_mov_b32 s27, 1
	s_cbranch_execz .LBB0_437
	s_movk_i32 s12, 0x800
	s_movk_i32 s37, 0x400
	s_mov_b32 s27, 0
	s_mov_b32 s38, s11
	s_mov_b64 s[6:7], s[4:5]
	s_cbranch_execz .LBB0_431
	s_branch .LBB0_432
